# hyena filter epilogue: stage values in LDS per wave and write out coalesced (4 channel rows x 64B per store instead of 64 scattered dwords)
# speedup vs baseline: 1.0388x; 1.0220x over previous
;     ...
;         for (int k4 = 0; k4 < 16; ++k4) {
;             float wf[4], wb[4];
; #pragma unroll
;             for (int j = 0; j < 4; ++j) { wf[j] = w3[(k4 * 4 + j) * 1024 + tid]; wb[j] = w3[(k4 * 4 + j) * 1024 + 512 + tid]; }
; #pragma unroll
;             for (int pp = 0; pp < 16; ++pp) {
;                 const float4 hv = *(const float4*)&h2[(hp * 16 + pp) * 64 + k4 * 4];
;                 accf[pp] += hv.x * wf[0]; accf[pp] += hv.y * wf[1]; accf[pp] += hv.z * wf[2]; accf[pp] += hv.w * wf[3];
;                 accb[pp] += hv.x * wb[0]; accb[pp] += hv.y * wb[1]; accb[pp] += hv.z * wb[2]; accb[pp] += hv.w * wb[3];
;             }
;         }
; #pragma unroll
;         for (int pp = 0; pp < 16; ++pp) {
;             const int pos = p0 + hp * 16 + pp;
;             const float t = (float)pos / (float)(l - 1);
;             const float win = expf(-t * delta);
;             const float f = accf[pp] * win, b = accb[pp] * win;
;             HF[pos] = f; asum += fabsf(f);
;             if (pos >= 1) { HF[-pos] = b; asum += fabsf(b); }
.Lhy_last:
	v_mov_b32_e32 v63, s101
	s_add_i32 s101, s101, 16
	ds_read_b128 v[94:97], v63
	ds_read_b128 v[98:101], v63 offset:256
	s_waitcnt vmcnt(0)
	ds_read_b128 v[58:61], v63 offset:512
	s_waitcnt lgkmcnt(2)
	v_fmac_f32_e32 v54, v86, v94
	v_fmac_f32_e32 v56, v90, v94
	v_fmac_f32_e32 v54, v87, v95
	v_fmac_f32_e32 v56, v91, v95
	v_fmac_f32_e32 v54, v88, v96
	v_fmac_f32_e32 v56, v92, v96
	v_fmac_f32_e32 v54, v89, v97
	v_fmac_f32_e32 v56, v93, v97
	ds_read_b128 v[94:97], v63 offset:768
	s_waitcnt lgkmcnt(2)
	v_fmac_f32_e32 v55, v86, v98
	v_fmac_f32_e32 v57, v90, v98
	v_fmac_f32_e32 v55, v87, v99
	v_fmac_f32_e32 v57, v91, v99
	v_fmac_f32_e32 v55, v88, v100
	v_fmac_f32_e32 v57, v92, v100
	v_fmac_f32_e32 v55, v89, v101
	v_fmac_f32_e32 v57, v93, v101
	ds_read_b128 v[98:101], v63 offset:1024
	s_waitcnt lgkmcnt(2)
	v_fmac_f32_e32 v50, v86, v58
	v_fmac_f32_e32 v52, v90, v58
	v_fmac_f32_e32 v50, v87, v59
	v_fmac_f32_e32 v52, v91, v59
	v_fmac_f32_e32 v50, v88, v60
	v_fmac_f32_e32 v52, v92, v60
	v_fmac_f32_e32 v50, v89, v61
	v_fmac_f32_e32 v52, v93, v61
	ds_read_b128 v[58:61], v63 offset:1280
	s_waitcnt lgkmcnt(2)
	v_fmac_f32_e32 v51, v86, v94
	v_fmac_f32_e32 v53, v90, v94
	v_fmac_f32_e32 v51, v87, v95
	v_fmac_f32_e32 v53, v91, v95
	v_fmac_f32_e32 v51, v88, v96
	v_fmac_f32_e32 v53, v92, v96
	v_fmac_f32_e32 v51, v89, v97
	v_fmac_f32_e32 v53, v93, v97
	ds_read_b128 v[94:97], v63 offset:1536
	s_waitcnt lgkmcnt(2)
	v_fmac_f32_e32 v46, v86, v98
	v_fmac_f32_e32 v48, v90, v98
	v_fmac_f32_e32 v46, v87, v99
	v_fmac_f32_e32 v48, v91, v99
	v_fmac_f32_e32 v46, v88, v100
	v_fmac_f32_e32 v48, v92, v100
	v_fmac_f32_e32 v46, v89, v101
	v_fmac_f32_e32 v48, v93, v101
	ds_read_b128 v[98:101], v63 offset:1792
	s_waitcnt lgkmcnt(2)
	v_fmac_f32_e32 v47, v86, v58
	v_fmac_f32_e32 v49, v90, v58
	v_fmac_f32_e32 v47, v87, v59
	v_fmac_f32_e32 v49, v91, v59
	v_fmac_f32_e32 v47, v88, v60
	v_fmac_f32_e32 v49, v92, v60
	v_fmac_f32_e32 v47, v89, v61
	v_fmac_f32_e32 v49, v93, v61
	ds_read_b128 v[58:61], v63 offset:2048
	s_waitcnt lgkmcnt(2)
	v_fmac_f32_e32 v42, v86, v94
	v_fmac_f32_e32 v44, v90, v94
	v_fmac_f32_e32 v42, v87, v95
	v_fmac_f32_e32 v44, v91, v95
	v_fmac_f32_e32 v42, v88, v96
	v_fmac_f32_e32 v44, v92, v96
	v_fmac_f32_e32 v42, v89, v97
	v_fmac_f32_e32 v44, v93, v97
	ds_read_b128 v[94:97], v63 offset:2304
	s_waitcnt lgkmcnt(2)
	v_fmac_f32_e32 v43, v86, v98
	v_fmac_f32_e32 v45, v90, v98
	v_fmac_f32_e32 v43, v87, v99
	v_fmac_f32_e32 v45, v91, v99
	v_fmac_f32_e32 v43, v88, v100
	v_fmac_f32_e32 v45, v92, v100
	v_fmac_f32_e32 v43, v89, v101
	v_fmac_f32_e32 v45, v93, v101
	ds_read_b128 v[98:101], v63 offset:2560
	s_waitcnt lgkmcnt(2)
	v_fmac_f32_e32 v38, v86, v58
	v_fmac_f32_e32 v40, v90, v58
	v_fmac_f32_e32 v38, v87, v59
	v_fmac_f32_e32 v40, v91, v59
	v_fmac_f32_e32 v38, v88, v60
	v_fmac_f32_e32 v40, v92, v60
	v_fmac_f32_e32 v38, v89, v61
	v_fmac_f32_e32 v40, v93, v61
	ds_read_b128 v[58:61], v63 offset:2816
	s_waitcnt lgkmcnt(2)
	v_fmac_f32_e32 v39, v86, v94
	v_fmac_f32_e32 v41, v90, v94
	v_fmac_f32_e32 v39, v87, v95
	v_fmac_f32_e32 v41, v91, v95
	v_fmac_f32_e32 v39, v88, v96
	v_fmac_f32_e32 v41, v92, v96
	v_fmac_f32_e32 v39, v89, v97
	v_fmac_f32_e32 v41, v93, v97
	ds_read_b128 v[94:97], v63 offset:3072
	s_waitcnt lgkmcnt(2)
	v_fmac_f32_e32 v34, v86, v98
	v_fmac_f32_e32 v36, v90, v98
	v_fmac_f32_e32 v34, v87, v99
	v_fmac_f32_e32 v36, v91, v99
	v_fmac_f32_e32 v34, v88, v100
	v_fmac_f32_e32 v36, v92, v100
	v_fmac_f32_e32 v34, v89, v101
	v_fmac_f32_e32 v36, v93, v101
	ds_read_b128 v[98:101], v63 offset:3328
	s_waitcnt lgkmcnt(2)
	v_fmac_f32_e32 v35, v86, v58
	v_fmac_f32_e32 v37, v90, v58
	v_fmac_f32_e32 v35, v87, v59
	v_fmac_f32_e32 v37, v91, v59
	v_fmac_f32_e32 v35, v88, v60
	v_fmac_f32_e32 v37, v92, v60
	v_fmac_f32_e32 v35, v89, v61
	v_fmac_f32_e32 v37, v93, v61
	ds_read_b128 v[58:61], v63 offset:3584
	s_waitcnt lgkmcnt(2)
	v_fmac_f32_e32 v30, v86, v94
	v_fmac_f32_e32 v32, v90, v94
	v_fmac_f32_e32 v30, v87, v95
	v_fmac_f32_e32 v32, v91, v95
	v_fmac_f32_e32 v30, v88, v96
	v_fmac_f32_e32 v32, v92, v96
	v_fmac_f32_e32 v30, v89, v97
	v_fmac_f32_e32 v32, v93, v97
	ds_read_b128 v[94:97], v63 offset:3840
	s_waitcnt lgkmcnt(2)
	v_fmac_f32_e32 v31, v86, v98
	v_fmac_f32_e32 v33, v90, v98
	v_fmac_f32_e32 v31, v87, v99
	v_fmac_f32_e32 v33, v91, v99
	v_fmac_f32_e32 v31, v88, v100
	v_fmac_f32_e32 v33, v92, v100
	v_fmac_f32_e32 v31, v89, v101
	v_fmac_f32_e32 v33, v93, v101
	s_waitcnt lgkmcnt(1)
	v_fmac_f32_e32 v26, v86, v58
	v_fmac_f32_e32 v28, v90, v58
	v_fmac_f32_e32 v26, v87, v59
	v_fmac_f32_e32 v28, v91, v59
	v_fmac_f32_e32 v26, v88, v60
	v_fmac_f32_e32 v28, v92, v60
	v_fmac_f32_e32 v26, v89, v61
	v_fmac_f32_e32 v28, v93, v61
	s_waitcnt lgkmcnt(0)
	v_fmac_f32_e32 v27, v86, v94
	v_fmac_f32_e32 v29, v90, v94
	v_fmac_f32_e32 v27, v87, v95
	v_fmac_f32_e32 v29, v91, v95
	v_fmac_f32_e32 v27, v88, v96
	v_fmac_f32_e32 v29, v92, v96
	v_fmac_f32_e32 v27, v89, v97
	v_fmac_f32_e32 v29, v93, v97
	v_lshrrev_b32_e32 v78, 6, v0
	v_and_b32_e32 v79, 63, v0
	v_mul_u32_u24_e32 v78, 0x2100, v78
	v_mul_u32_u24_e32 v79, 0x84, v79
	v_add_u32_e32 v78, v78, v79
	v_add_u32_e32 v78, 0xa000, v78
	s_lshl_b32 s2, s7, 4
	s_or_b32 s2, s2, s15
	v_cvt_f32_i32_e32 v2, s2
	s_ashr_i32 s3, s2, 31
	s_cmp_gt_i32 s2, 0
	v_div_scale_f32 v3, s[4:5], v77, v77, -v2
	v_rcp_f32_e32 v4, v3
	v_div_scale_f32 v5, vcc, -v2, v77, -v2
	v_fma_f32 v58, -v3, v4, 1.0
	v_fmac_f32_e32 v4, v58, v4
	v_mul_f32_e32 v58, v5, v4
	v_fma_f32 v59, -v3, v58, v5
	v_fmac_f32_e32 v58, v59, v4
	v_fma_f32 v3, -v3, v58, v5
	v_div_fmas_f32 v3, v3, v4, v58
	v_div_fixup_f32 v2, v3, v77, -v2
	v_mul_f32_e64 v2, |v67|, v2
	v_mul_f32_e32 v3, 0x3fb8aa3b, v2
	v_fma_f32 v4, v2, s40, -v3
	v_rndne_f32_e32 v5, v3
	v_fmac_f32_e32 v4, 0x32a5705f, v2
	v_sub_f32_e32 v3, v3, v5
	v_add_f32_e32 v3, v3, v4
	v_cvt_i32_f32_e32 v4, v5
	v_exp_f32_e32 v3, v3
	v_cmp_ngt_f32_e32 vcc, s41, v2
	v_ldexp_f32 v3, v3, v4
	s_nop 0
	v_cndmask_b32_e32 v3, 0, v3, vcc
	v_cmp_nlt_f32_e32 vcc, s42, v2
	s_nop 1
	v_cndmask_b32_e32 v5, v76, v3, vcc
	v_mul_f32_e32 v4, v5, v54
	v_lshl_add_u64 v[2:3], s[2:3], 2, v[24:25]
	ds_write_b32 v78, v4 offset:0
	v_add_f32_e64 v4, v22, |v4|
	s_cbranch_scc0 .LBB0_79
	s_sub_i32 s4, 0, s2
	v_mul_f32_e32 v5, v5, v56
	s_ashr_i32 s5, s4, 31
	v_add_f32_e64 v4, |v5|, v4
	v_lshl_add_u64 v[58:59], s[4:5], 2, v[24:25]
	ds_write_b32 v78, v5 offset:124
;     ...
; #pragma unroll
;         for (int pp = 0; pp < 16; ++pp) {
;             const int pos = p0 + hp * 16 + pp;
;             const float t = (float)pos / (float)(l - 1);
;             const float win = expf(-t * delta);
;             const float f = accf[pp] * win, b = accb[pp] * win;
;             HF[pos] = f; asum += fabsf(f);
;             if (pos >= 1) { HF[-pos] = b; asum += fabsf(b); }
;         }
.LBB0_79:
	s_or_b32 s4, s2, 1
	v_cvt_f32_i32_e32 v5, s4
	v_div_scale_f32 v22, s[4:5], v77, v77, -v5
	v_rcp_f32_e32 v54, v22
	v_div_scale_f32 v56, vcc, -v5, v77, -v5
	v_fma_f32 v58, -v22, v54, 1.0
	v_fmac_f32_e32 v54, v58, v54
	v_mul_f32_e32 v58, v56, v54
	v_fma_f32 v59, -v22, v58, v56
	v_fmac_f32_e32 v58, v59, v54
	v_fma_f32 v22, -v22, v58, v56
	v_div_fmas_f32 v22, v22, v54, v58
	v_div_fixup_f32 v5, v22, v77, -v5
	v_mul_f32_e64 v5, |v67|, v5
	v_mul_f32_e32 v22, 0x3fb8aa3b, v5
	v_fma_f32 v54, v5, s40, -v22
	v_rndne_f32_e32 v56, v22
	v_fmac_f32_e32 v54, 0x32a5705f, v5
	v_sub_f32_e32 v22, v22, v56
	v_add_f32_e32 v22, v22, v54
	v_cvt_i32_f32_e32 v54, v56
	v_exp_f32_e32 v22, v22
	v_cmp_ngt_f32_e32 vcc, s41, v5
	v_ldexp_f32 v22, v22, v54
	s_nop 0
	v_cndmask_b32_e32 v22, 0, v22, vcc
	v_cmp_nlt_f32_e32 vcc, s42, v5
	v_cndmask_b32_e64 v54, 0, 1, s[0:1]
	v_cmp_ne_u32_e64 s[6:7], 1, v54
	v_cndmask_b32_e32 v5, v76, v22, vcc
	v_mul_f32_e32 v22, v5, v55
	s_andn2_b64 vcc, exec, s[0:1]
	v_add_f32_e64 v4, |v22|, v4
	ds_write_b32 v78, v22 offset:4
	s_cbranch_vccnz .LBB0_81
	s_lshl_b64 s[4:5], s[2:3], 2
	v_mul_f32_e32 v5, v5, v57
	v_mov_b32_e32 v22, s5
	v_subrev_co_u32_e32 v54, vcc, s4, v24
	v_add_f32_e64 v4, |v5|, v4
	s_nop 0
	v_subb_co_u32_e32 v55, vcc, v25, v22, vcc
	ds_write_b32 v78, v5 offset:120
.LBB0_81:
	s_or_b32 s4, s2, 2
	v_cvt_f32_i32_e32 v5, s4
	v_div_scale_f32 v22, s[4:5], v77, v77, -v5
	v_rcp_f32_e32 v54, v22
	v_div_scale_f32 v55, vcc, -v5, v77, -v5
	v_fma_f32 v56, -v22, v54, 1.0
	v_fmac_f32_e32 v54, v56, v54
	v_mul_f32_e32 v56, v55, v54
	v_fma_f32 v57, -v22, v56, v55
	v_fmac_f32_e32 v56, v57, v54
	v_fma_f32 v22, -v22, v56, v55
	v_div_fmas_f32 v22, v22, v54, v56
	v_div_fixup_f32 v5, v22, v77, -v5
	v_mul_f32_e64 v5, |v67|, v5
	v_mul_f32_e32 v22, 0x3fb8aa3b, v5
	v_fma_f32 v54, v5, s40, -v22
	v_rndne_f32_e32 v55, v22
	v_fmac_f32_e32 v54, 0x32a5705f, v5
	v_sub_f32_e32 v22, v22, v55
	v_add_f32_e32 v22, v22, v54
	v_cvt_i32_f32_e32 v54, v55
	v_exp_f32_e32 v22, v22
	v_cmp_ngt_f32_e32 vcc, s41, v5
	v_ldexp_f32 v22, v22, v54
	s_nop 0
	v_cndmask_b32_e32 v22, 0, v22, vcc
	v_cmp_nlt_f32_e32 vcc, s42, v5
	s_nop 1
	v_cndmask_b32_e32 v5, v76, v22, vcc
	v_mul_f32_e32 v22, v5, v50
	s_and_b64 vcc, exec, s[6:7]
	v_add_f32_e64 v4, |v22|, v4
	ds_write_b32 v78, v22 offset:8
	s_cbranch_vccnz .LBB0_83
	s_lshl_b64 s[4:5], s[2:3], 2
	v_mul_f32_e32 v5, v5, v52
	v_mov_b32_e32 v22, s5
	v_subrev_co_u32_e32 v54, vcc, s4, v24
	v_add_f32_e64 v4, |v5|, v4
	s_nop 0
	v_subb_co_u32_e32 v55, vcc, v25, v22, vcc
	ds_write_b32 v78, v5 offset:116
.LBB0_83:
	s_or_b32 s4, s2, 3
	v_cvt_f32_i32_e32 v5, s4
	v_div_scale_f32 v22, s[4:5], v77, v77, -v5
	v_rcp_f32_e32 v50, v22
	v_div_scale_f32 v52, vcc, -v5, v77, -v5
	v_fma_f32 v54, -v22, v50, 1.0
	v_fmac_f32_e32 v50, v54, v50
	v_mul_f32_e32 v54, v52, v50
	v_fma_f32 v55, -v22, v54, v52
	v_fmac_f32_e32 v54, v55, v50
	v_fma_f32 v22, -v22, v54, v52
	v_div_fmas_f32 v22, v22, v50, v54
	v_div_fixup_f32 v5, v22, v77, -v5
	v_mul_f32_e64 v5, |v67|, v5
	v_mul_f32_e32 v22, 0x3fb8aa3b, v5
	v_fma_f32 v50, v5, s40, -v22
	v_rndne_f32_e32 v52, v22
	v_fmac_f32_e32 v50, 0x32a5705f, v5
	v_sub_f32_e32 v22, v22, v52
	v_add_f32_e32 v22, v22, v50
	v_cvt_i32_f32_e32 v50, v52
	v_exp_f32_e32 v22, v22
	v_cmp_ngt_f32_e32 vcc, s41, v5
	v_ldexp_f32 v22, v22, v50
	s_nop 0
	v_cndmask_b32_e32 v22, 0, v22, vcc
	v_cmp_nlt_f32_e32 vcc, s42, v5
	s_nop 1
	v_cndmask_b32_e32 v5, v76, v22, vcc
	v_mul_f32_e32 v22, v5, v51
	s_and_b64 vcc, exec, s[6:7]
	v_add_f32_e64 v4, |v22|, v4
	ds_write_b32 v78, v22 offset:12
	s_cbranch_vccnz .LBB0_85
	s_lshl_b64 s[4:5], s[2:3], 2
	v_mul_f32_e32 v5, v5, v53
	v_mov_b32_e32 v22, s5
	v_subrev_co_u32_e32 v50, vcc, s4, v24
	v_add_f32_e64 v4, |v5|, v4
	s_nop 0
	v_subb_co_u32_e32 v51, vcc, v25, v22, vcc
	ds_write_b32 v78, v5 offset:112
.LBB0_85:
	s_or_b32 s4, s2, 4
	v_cvt_f32_i32_e32 v5, s4
	v_div_scale_f32 v22, s[4:5], v77, v77, -v5
	v_rcp_f32_e32 v50, v22
	v_div_scale_f32 v51, vcc, -v5, v77, -v5
	v_fma_f32 v52, -v22, v50, 1.0
	v_fmac_f32_e32 v50, v52, v50
	v_mul_f32_e32 v52, v51, v50
	v_fma_f32 v53, -v22, v52, v51
	v_fmac_f32_e32 v52, v53, v50
	v_fma_f32 v22, -v22, v52, v51
	v_div_fmas_f32 v22, v22, v50, v52
	v_div_fixup_f32 v5, v22, v77, -v5
	v_mul_f32_e64 v5, |v67|, v5
	v_mul_f32_e32 v22, 0x3fb8aa3b, v5
	v_fma_f32 v50, v5, s40, -v22
	v_rndne_f32_e32 v51, v22
	v_fmac_f32_e32 v50, 0x32a5705f, v5
	v_sub_f32_e32 v22, v22, v51
	v_add_f32_e32 v22, v22, v50
	v_cvt_i32_f32_e32 v50, v51
	v_exp_f32_e32 v22, v22
	v_cmp_ngt_f32_e32 vcc, s41, v5
	v_ldexp_f32 v22, v22, v50
	s_nop 0
	v_cndmask_b32_e32 v22, 0, v22, vcc
	v_cmp_nlt_f32_e32 vcc, s42, v5
	s_nop 1
	v_cndmask_b32_e32 v5, v76, v22, vcc
	v_mul_f32_e32 v22, v5, v46
	s_and_b64 vcc, exec, s[6:7]
	v_add_f32_e64 v4, |v22|, v4
	ds_write_b32 v78, v22 offset:16
	s_cbranch_vccnz .LBB0_87
	s_lshl_b64 s[4:5], s[2:3], 2
	v_mul_f32_e32 v5, v5, v48
	v_mov_b32_e32 v22, s5
	v_subrev_co_u32_e32 v50, vcc, s4, v24
	v_add_f32_e64 v4, |v5|, v4
	s_nop 0
	v_subb_co_u32_e32 v51, vcc, v25, v22, vcc
	ds_write_b32 v78, v5 offset:108
;     ...
; #pragma unroll
;         for (int pp = 0; pp < 16; ++pp) {
;             const int pos = p0 + hp * 16 + pp;
;             const float t = (float)pos / (float)(l - 1);
;             const float win = expf(-t * delta);
;             const float f = accf[pp] * win, b = accb[pp] * win;
;             HF[pos] = f; asum += fabsf(f);
;             if (pos >= 1) { HF[-pos] = b; asum += fabsf(b); }
;         }
.LBB0_87:
	s_or_b32 s4, s2, 5
	v_cvt_f32_i32_e32 v5, s4
	v_div_scale_f32 v22, s[4:5], v77, v77, -v5
	v_rcp_f32_e32 v46, v22
	v_div_scale_f32 v48, vcc, -v5, v77, -v5
	v_fma_f32 v50, -v22, v46, 1.0
	v_fmac_f32_e32 v46, v50, v46
	v_mul_f32_e32 v50, v48, v46
	v_fma_f32 v51, -v22, v50, v48
	v_fmac_f32_e32 v50, v51, v46
	v_fma_f32 v22, -v22, v50, v48
	v_div_fmas_f32 v22, v22, v46, v50
	v_div_fixup_f32 v5, v22, v77, -v5
	v_mul_f32_e64 v5, |v67|, v5
	v_mul_f32_e32 v22, 0x3fb8aa3b, v5
	v_fma_f32 v46, v5, s40, -v22
	v_rndne_f32_e32 v48, v22
	v_fmac_f32_e32 v46, 0x32a5705f, v5
	v_sub_f32_e32 v22, v22, v48
	v_add_f32_e32 v22, v22, v46
	v_cvt_i32_f32_e32 v46, v48
	v_exp_f32_e32 v22, v22
	v_cmp_ngt_f32_e32 vcc, s41, v5
	v_ldexp_f32 v22, v22, v46
	s_nop 0
	v_cndmask_b32_e32 v22, 0, v22, vcc
	v_cmp_nlt_f32_e32 vcc, s42, v5
	s_nop 1
	v_cndmask_b32_e32 v5, v76, v22, vcc
	v_mul_f32_e32 v22, v5, v47
	s_and_b64 vcc, exec, s[6:7]
	v_add_f32_e64 v4, |v22|, v4
	ds_write_b32 v78, v22 offset:20
	s_cbranch_vccnz .LBB0_89
	s_lshl_b64 s[4:5], s[2:3], 2
	v_mul_f32_e32 v5, v5, v49
	v_mov_b32_e32 v22, s5
	v_subrev_co_u32_e32 v46, vcc, s4, v24
	v_add_f32_e64 v4, |v5|, v4
	s_nop 0
	v_subb_co_u32_e32 v47, vcc, v25, v22, vcc
	ds_write_b32 v78, v5 offset:104
.LBB0_89:
	s_or_b32 s4, s2, 6
	v_cvt_f32_i32_e32 v5, s4
	v_div_scale_f32 v22, s[4:5], v77, v77, -v5
	v_rcp_f32_e32 v46, v22
	v_div_scale_f32 v47, vcc, -v5, v77, -v5
	v_fma_f32 v48, -v22, v46, 1.0
	v_fmac_f32_e32 v46, v48, v46
	v_mul_f32_e32 v48, v47, v46
	v_fma_f32 v49, -v22, v48, v47
	v_fmac_f32_e32 v48, v49, v46
	v_fma_f32 v22, -v22, v48, v47
	v_div_fmas_f32 v22, v22, v46, v48
	v_div_fixup_f32 v5, v22, v77, -v5
	v_mul_f32_e64 v5, |v67|, v5
	v_mul_f32_e32 v22, 0x3fb8aa3b, v5
	v_fma_f32 v46, v5, s40, -v22
	v_rndne_f32_e32 v47, v22
	v_fmac_f32_e32 v46, 0x32a5705f, v5
	v_sub_f32_e32 v22, v22, v47
	v_add_f32_e32 v22, v22, v46
	v_cvt_i32_f32_e32 v46, v47
	v_exp_f32_e32 v22, v22
	v_cmp_ngt_f32_e32 vcc, s41, v5
	v_ldexp_f32 v22, v22, v46
	s_nop 0
	v_cndmask_b32_e32 v22, 0, v22, vcc
	v_cmp_nlt_f32_e32 vcc, s42, v5
	s_nop 1
	v_cndmask_b32_e32 v5, v76, v22, vcc
	v_mul_f32_e32 v22, v5, v42
	s_and_b64 vcc, exec, s[6:7]
	v_add_f32_e64 v4, |v22|, v4
	ds_write_b32 v78, v22 offset:24
	s_cbranch_vccnz .LBB0_91
	s_lshl_b64 s[4:5], s[2:3], 2
	v_mul_f32_e32 v5, v5, v44
	v_mov_b32_e32 v22, s5
	v_subrev_co_u32_e32 v46, vcc, s4, v24
	v_add_f32_e64 v4, |v5|, v4
	s_nop 0
	v_subb_co_u32_e32 v47, vcc, v25, v22, vcc
	ds_write_b32 v78, v5 offset:100
.LBB0_91:
	s_or_b32 s4, s2, 7
	v_cvt_f32_i32_e32 v5, s4
	v_div_scale_f32 v22, s[4:5], v77, v77, -v5
	v_rcp_f32_e32 v42, v22
	v_div_scale_f32 v44, vcc, -v5, v77, -v5
	v_fma_f32 v46, -v22, v42, 1.0
	v_fmac_f32_e32 v42, v46, v42
	v_mul_f32_e32 v46, v44, v42
	v_fma_f32 v47, -v22, v46, v44
	v_fmac_f32_e32 v46, v47, v42
	v_fma_f32 v22, -v22, v46, v44
	v_div_fmas_f32 v22, v22, v42, v46
	v_div_fixup_f32 v5, v22, v77, -v5
	v_mul_f32_e64 v5, |v67|, v5
	v_mul_f32_e32 v22, 0x3fb8aa3b, v5
	v_fma_f32 v42, v5, s40, -v22
	v_rndne_f32_e32 v44, v22
	v_fmac_f32_e32 v42, 0x32a5705f, v5
	v_sub_f32_e32 v22, v22, v44
	v_add_f32_e32 v22, v22, v42
	v_cvt_i32_f32_e32 v42, v44
	v_exp_f32_e32 v22, v22
	v_cmp_ngt_f32_e32 vcc, s41, v5
	v_ldexp_f32 v22, v22, v42
	s_nop 0
	v_cndmask_b32_e32 v22, 0, v22, vcc
	v_cmp_nlt_f32_e32 vcc, s42, v5
	s_nop 1
	v_cndmask_b32_e32 v5, v76, v22, vcc
	v_mul_f32_e32 v22, v5, v43
	s_and_b64 vcc, exec, s[6:7]
	v_add_f32_e64 v4, |v22|, v4
	ds_write_b32 v78, v22 offset:28
	s_cbranch_vccnz .LBB0_93
	s_lshl_b64 s[4:5], s[2:3], 2
	v_mul_f32_e32 v5, v5, v45
	v_mov_b32_e32 v22, s5
	v_subrev_co_u32_e32 v42, vcc, s4, v24
	v_add_f32_e64 v4, |v5|, v4
	s_nop 0
	v_subb_co_u32_e32 v43, vcc, v25, v22, vcc
	ds_write_b32 v78, v5 offset:96
.LBB0_93:
	s_or_b32 s4, s2, 8
	v_cvt_f32_i32_e32 v5, s4
	v_div_scale_f32 v22, s[4:5], v77, v77, -v5
	v_rcp_f32_e32 v42, v22
	v_div_scale_f32 v43, vcc, -v5, v77, -v5
	v_fma_f32 v44, -v22, v42, 1.0
	v_fmac_f32_e32 v42, v44, v42
	v_mul_f32_e32 v44, v43, v42
	v_fma_f32 v45, -v22, v44, v43
	v_fmac_f32_e32 v44, v45, v42
	v_fma_f32 v22, -v22, v44, v43
	v_div_fmas_f32 v22, v22, v42, v44
	v_div_fixup_f32 v5, v22, v77, -v5
	v_mul_f32_e64 v5, |v67|, v5
	v_mul_f32_e32 v22, 0x3fb8aa3b, v5
	v_fma_f32 v42, v5, s40, -v22
	v_rndne_f32_e32 v43, v22
	v_fmac_f32_e32 v42, 0x32a5705f, v5
	v_sub_f32_e32 v22, v22, v43
	v_add_f32_e32 v22, v22, v42
	v_cvt_i32_f32_e32 v42, v43
	v_exp_f32_e32 v22, v22
	v_cmp_ngt_f32_e32 vcc, s41, v5
	v_ldexp_f32 v22, v22, v42
	s_nop 0
	v_cndmask_b32_e32 v22, 0, v22, vcc
	v_cmp_nlt_f32_e32 vcc, s42, v5
	s_nop 1
	v_cndmask_b32_e32 v5, v76, v22, vcc
	v_mul_f32_e32 v22, v5, v38
	s_and_b64 vcc, exec, s[6:7]
	v_add_f32_e64 v4, |v22|, v4
	ds_write_b32 v78, v22 offset:32
	s_cbranch_vccnz .LBB0_95
	s_lshl_b64 s[4:5], s[2:3], 2
	v_mul_f32_e32 v5, v5, v40
	v_mov_b32_e32 v22, s5
	v_subrev_co_u32_e32 v42, vcc, s4, v24
	v_add_f32_e64 v4, |v5|, v4
	s_nop 0
	v_subb_co_u32_e32 v43, vcc, v25, v22, vcc
	ds_write_b32 v78, v5 offset:92
.LBB0_95:
	s_or_b32 s4, s2, 9
	v_cvt_f32_i32_e32 v5, s4
	v_div_scale_f32 v22, s[4:5], v77, v77, -v5
	v_rcp_f32_e32 v38, v22
	v_div_scale_f32 v40, vcc, -v5, v77, -v5
	v_fma_f32 v42, -v22, v38, 1.0
	v_fmac_f32_e32 v38, v42, v38
	v_mul_f32_e32 v42, v40, v38
	v_fma_f32 v43, -v22, v42, v40
	v_fmac_f32_e32 v42, v43, v38
	v_fma_f32 v22, -v22, v42, v40
	v_div_fmas_f32 v22, v22, v38, v42
	v_div_fixup_f32 v5, v22, v77, -v5
	v_mul_f32_e64 v5, |v67|, v5
	v_mul_f32_e32 v22, 0x3fb8aa3b, v5
	v_fma_f32 v38, v5, s40, -v22
	v_rndne_f32_e32 v40, v22
	v_fmac_f32_e32 v38, 0x32a5705f, v5
	v_sub_f32_e32 v22, v22, v40
	v_add_f32_e32 v22, v22, v38
	v_cvt_i32_f32_e32 v38, v40
	v_exp_f32_e32 v22, v22
	v_cmp_ngt_f32_e32 vcc, s41, v5
	v_ldexp_f32 v22, v22, v38
	s_nop 0
	v_cndmask_b32_e32 v22, 0, v22, vcc
	v_cmp_nlt_f32_e32 vcc, s42, v5
	s_nop 1
	v_cndmask_b32_e32 v5, v76, v22, vcc
	v_mul_f32_e32 v22, v5, v39
	s_and_b64 vcc, exec, s[6:7]
	v_add_f32_e64 v4, |v22|, v4
	ds_write_b32 v78, v22 offset:36
	s_cbranch_vccnz .LBB0_97
	s_lshl_b64 s[4:5], s[2:3], 2
	v_mul_f32_e32 v5, v5, v41
	v_mov_b32_e32 v22, s5
	v_subrev_co_u32_e32 v38, vcc, s4, v24
	v_add_f32_e64 v4, |v5|, v4
	s_nop 0
	v_subb_co_u32_e32 v39, vcc, v25, v22, vcc
	ds_write_b32 v78, v5 offset:88
;     ...
; #pragma unroll
;         for (int pp = 0; pp < 16; ++pp) {
;             const int pos = p0 + hp * 16 + pp;
;             const float t = (float)pos / (float)(l - 1);
;             const float win = expf(-t * delta);
;             const float f = accf[pp] * win, b = accb[pp] * win;
;             HF[pos] = f; asum += fabsf(f);
;             if (pos >= 1) { HF[-pos] = b; asum += fabsf(b); }
;         }
.LBB0_97:
	s_or_b32 s4, s2, 10
	v_cvt_f32_i32_e32 v5, s4
	v_div_scale_f32 v22, s[4:5], v77, v77, -v5
	v_rcp_f32_e32 v38, v22
	v_div_scale_f32 v39, vcc, -v5, v77, -v5
	v_fma_f32 v40, -v22, v38, 1.0
	v_fmac_f32_e32 v38, v40, v38
	v_mul_f32_e32 v40, v39, v38
	v_fma_f32 v41, -v22, v40, v39
	v_fmac_f32_e32 v40, v41, v38
	v_fma_f32 v22, -v22, v40, v39
	v_div_fmas_f32 v22, v22, v38, v40
	v_div_fixup_f32 v5, v22, v77, -v5
	v_mul_f32_e64 v5, |v67|, v5
	v_mul_f32_e32 v22, 0x3fb8aa3b, v5
	v_fma_f32 v38, v5, s40, -v22
	v_rndne_f32_e32 v39, v22
	v_fmac_f32_e32 v38, 0x32a5705f, v5
	v_sub_f32_e32 v22, v22, v39
	v_add_f32_e32 v22, v22, v38
	v_cvt_i32_f32_e32 v38, v39
	v_exp_f32_e32 v22, v22
	v_cmp_ngt_f32_e32 vcc, s41, v5
	v_ldexp_f32 v22, v22, v38
	s_nop 0
	v_cndmask_b32_e32 v22, 0, v22, vcc
	v_cmp_nlt_f32_e32 vcc, s42, v5
	s_nop 1
	v_cndmask_b32_e32 v5, v76, v22, vcc
	v_mul_f32_e32 v22, v5, v34
	s_and_b64 vcc, exec, s[6:7]
	v_add_f32_e64 v4, |v22|, v4
	ds_write_b32 v78, v22 offset:40
	s_cbranch_vccnz .LBB0_99
	s_lshl_b64 s[4:5], s[2:3], 2
	v_mul_f32_e32 v5, v5, v36
	v_mov_b32_e32 v22, s5
	v_subrev_co_u32_e32 v38, vcc, s4, v24
	v_add_f32_e64 v4, |v5|, v4
	s_nop 0
	v_subb_co_u32_e32 v39, vcc, v25, v22, vcc
	ds_write_b32 v78, v5 offset:84
.LBB0_99:
	s_or_b32 s4, s2, 11
	v_cvt_f32_i32_e32 v5, s4
	v_div_scale_f32 v22, s[4:5], v77, v77, -v5
	v_rcp_f32_e32 v34, v22
	v_div_scale_f32 v36, vcc, -v5, v77, -v5
	v_fma_f32 v38, -v22, v34, 1.0
	v_fmac_f32_e32 v34, v38, v34
	v_mul_f32_e32 v38, v36, v34
	v_fma_f32 v39, -v22, v38, v36
	v_fmac_f32_e32 v38, v39, v34
	v_fma_f32 v22, -v22, v38, v36
	v_div_fmas_f32 v22, v22, v34, v38
	v_div_fixup_f32 v5, v22, v77, -v5
	v_mul_f32_e64 v5, |v67|, v5
	v_mul_f32_e32 v22, 0x3fb8aa3b, v5
	v_fma_f32 v34, v5, s40, -v22
	v_rndne_f32_e32 v36, v22
	v_fmac_f32_e32 v34, 0x32a5705f, v5
	v_sub_f32_e32 v22, v22, v36
	v_add_f32_e32 v22, v22, v34
	v_cvt_i32_f32_e32 v34, v36
	v_exp_f32_e32 v22, v22
	v_cmp_ngt_f32_e32 vcc, s41, v5
	v_ldexp_f32 v22, v22, v34
	s_nop 0
	v_cndmask_b32_e32 v22, 0, v22, vcc
	v_cmp_nlt_f32_e32 vcc, s42, v5
	s_nop 1
	v_cndmask_b32_e32 v5, v76, v22, vcc
	v_mul_f32_e32 v22, v5, v35
	s_and_b64 vcc, exec, s[6:7]
	v_add_f32_e64 v4, |v22|, v4
	ds_write_b32 v78, v22 offset:44
	s_cbranch_vccnz .LBB0_101
	s_lshl_b64 s[4:5], s[2:3], 2
	v_mul_f32_e32 v5, v5, v37
	v_mov_b32_e32 v22, s5
	v_subrev_co_u32_e32 v34, vcc, s4, v24
	v_add_f32_e64 v4, |v5|, v4
	s_nop 0
	v_subb_co_u32_e32 v35, vcc, v25, v22, vcc
	ds_write_b32 v78, v5 offset:80
.LBB0_101:
	s_or_b32 s4, s2, 12
	v_cvt_f32_i32_e32 v5, s4
	v_div_scale_f32 v22, s[4:5], v77, v77, -v5
	v_rcp_f32_e32 v34, v22
	v_div_scale_f32 v35, vcc, -v5, v77, -v5
	v_fma_f32 v36, -v22, v34, 1.0
	v_fmac_f32_e32 v34, v36, v34
	v_mul_f32_e32 v36, v35, v34
	v_fma_f32 v37, -v22, v36, v35
	v_fmac_f32_e32 v36, v37, v34
	v_fma_f32 v22, -v22, v36, v35
	v_div_fmas_f32 v22, v22, v34, v36
	v_div_fixup_f32 v5, v22, v77, -v5
	v_mul_f32_e64 v5, |v67|, v5
	v_mul_f32_e32 v22, 0x3fb8aa3b, v5
	v_fma_f32 v34, v5, s40, -v22
	v_rndne_f32_e32 v35, v22
	v_fmac_f32_e32 v34, 0x32a5705f, v5
	v_sub_f32_e32 v22, v22, v35
	v_add_f32_e32 v22, v22, v34
	v_cvt_i32_f32_e32 v34, v35
	v_exp_f32_e32 v22, v22
	v_cmp_ngt_f32_e32 vcc, s41, v5
	v_ldexp_f32 v22, v22, v34
	s_nop 0
	v_cndmask_b32_e32 v22, 0, v22, vcc
	v_cmp_nlt_f32_e32 vcc, s42, v5
	s_nop 1
	v_cndmask_b32_e32 v5, v76, v22, vcc
	v_mul_f32_e32 v22, v5, v30
	s_and_b64 vcc, exec, s[6:7]
	v_add_f32_e64 v4, |v22|, v4
	ds_write_b32 v78, v22 offset:48
	s_cbranch_vccnz .LBB0_103
	s_lshl_b64 s[4:5], s[2:3], 2
	v_mul_f32_e32 v5, v5, v32
	v_mov_b32_e32 v22, s5
	v_subrev_co_u32_e32 v34, vcc, s4, v24
	v_add_f32_e64 v4, |v5|, v4
	s_nop 0
	v_subb_co_u32_e32 v35, vcc, v25, v22, vcc
	ds_write_b32 v78, v5 offset:76
.LBB0_103:
	s_or_b32 s4, s2, 13
	v_cvt_f32_i32_e32 v5, s4
	v_div_scale_f32 v22, s[4:5], v77, v77, -v5
	v_rcp_f32_e32 v30, v22
	v_div_scale_f32 v32, vcc, -v5, v77, -v5
	v_fma_f32 v34, -v22, v30, 1.0
	v_fmac_f32_e32 v30, v34, v30
	v_mul_f32_e32 v34, v32, v30
	v_fma_f32 v35, -v22, v34, v32
	v_fmac_f32_e32 v34, v35, v30
	v_fma_f32 v22, -v22, v34, v32
	v_div_fmas_f32 v22, v22, v30, v34
	v_div_fixup_f32 v5, v22, v77, -v5
	v_mul_f32_e64 v5, |v67|, v5
	v_mul_f32_e32 v22, 0x3fb8aa3b, v5
	v_fma_f32 v30, v5, s40, -v22
	v_rndne_f32_e32 v32, v22
	v_fmac_f32_e32 v30, 0x32a5705f, v5
	v_sub_f32_e32 v22, v22, v32
	v_add_f32_e32 v22, v22, v30
	v_cvt_i32_f32_e32 v30, v32
	v_exp_f32_e32 v22, v22
	v_cmp_ngt_f32_e32 vcc, s41, v5
	v_ldexp_f32 v22, v22, v30
	s_nop 0
	v_cndmask_b32_e32 v22, 0, v22, vcc
	v_cmp_nlt_f32_e32 vcc, s42, v5
	s_nop 1
	v_cndmask_b32_e32 v5, v76, v22, vcc
	v_mul_f32_e32 v22, v5, v31
	s_and_b64 vcc, exec, s[6:7]
	v_add_f32_e64 v4, |v22|, v4
	ds_write_b32 v78, v22 offset:52
	s_cbranch_vccnz .LBB0_105
	s_lshl_b64 s[4:5], s[2:3], 2
	v_mul_f32_e32 v5, v5, v33
	v_mov_b32_e32 v22, s5
	v_subrev_co_u32_e32 v30, vcc, s4, v24
	v_add_f32_e64 v4, |v5|, v4
	s_nop 0
	v_subb_co_u32_e32 v31, vcc, v25, v22, vcc
	ds_write_b32 v78, v5 offset:72
.LBB0_105:
	s_or_b32 s4, s2, 14
	v_cvt_f32_i32_e32 v5, s4
	v_div_scale_f32 v22, s[4:5], v77, v77, -v5
	v_rcp_f32_e32 v30, v22
	v_div_scale_f32 v31, vcc, -v5, v77, -v5
	v_fma_f32 v32, -v22, v30, 1.0
	v_fmac_f32_e32 v30, v32, v30
	v_mul_f32_e32 v32, v31, v30
	v_fma_f32 v33, -v22, v32, v31
	v_fmac_f32_e32 v32, v33, v30
	v_fma_f32 v22, -v22, v32, v31
	v_div_fmas_f32 v22, v22, v30, v32
	v_div_fixup_f32 v5, v22, v77, -v5
	v_mul_f32_e64 v5, |v67|, v5
	v_mul_f32_e32 v22, 0x3fb8aa3b, v5
	v_fma_f32 v30, v5, s40, -v22
	v_rndne_f32_e32 v31, v22
	v_fmac_f32_e32 v30, 0x32a5705f, v5
	v_sub_f32_e32 v22, v22, v31
	v_add_f32_e32 v22, v22, v30
	v_cvt_i32_f32_e32 v30, v31
	v_exp_f32_e32 v22, v22
	v_cmp_ngt_f32_e32 vcc, s41, v5
	v_ldexp_f32 v22, v22, v30
	s_nop 0
	v_cndmask_b32_e32 v22, 0, v22, vcc
	v_cmp_nlt_f32_e32 vcc, s42, v5
	s_nop 1
	v_cndmask_b32_e32 v5, v76, v22, vcc
	v_mul_f32_e32 v22, v5, v26
	s_and_b64 vcc, exec, s[6:7]
	v_add_f32_e64 v4, |v22|, v4
	ds_write_b32 v78, v22 offset:56
	s_cbranch_vccnz .LBB0_107
	s_lshl_b64 s[4:5], s[2:3], 2
	v_mul_f32_e32 v5, v5, v28
	v_mov_b32_e32 v22, s5
	v_subrev_co_u32_e32 v30, vcc, s4, v24
	v_add_f32_e64 v4, |v5|, v4
	s_nop 0
	v_subb_co_u32_e32 v31, vcc, v25, v22, vcc
	ds_write_b32 v78, v5 offset:68
;     ...
;         for (int pp = 0; pp < 16; ++pp) {
;             const int pos = p0 + hp * 16 + pp;
;             const float t = (float)pos / (float)(l - 1);
;             const float win = expf(-t * delta);
;             const float f = accf[pp] * win, b = accb[pp] * win;
;             HF[pos] = f; asum += fabsf(f);
;             if (pos >= 1) { HF[-pos] = b; asum += fabsf(b); }
;         }
.LBB0_107:
	s_or_b32 s4, s2, 15
	v_cvt_f32_i32_e32 v5, s4
	v_div_scale_f32 v22, s[4:5], v77, v77, -v5
	v_rcp_f32_e32 v26, v22
	v_div_scale_f32 v28, vcc, -v5, v77, -v5
	v_fma_f32 v30, -v22, v26, 1.0
	v_fmac_f32_e32 v26, v30, v26
	v_mul_f32_e32 v30, v28, v26
	v_fma_f32 v31, -v22, v30, v28
	v_fmac_f32_e32 v30, v31, v26
	v_fma_f32 v22, -v22, v30, v28
	v_div_fmas_f32 v22, v22, v26, v30
	v_div_fixup_f32 v5, v22, v77, -v5
	v_mul_f32_e64 v5, |v67|, v5
	v_mul_f32_e32 v22, 0x3fb8aa3b, v5
	v_fma_f32 v26, v5, s40, -v22
	v_rndne_f32_e32 v28, v22
	v_fmac_f32_e32 v26, 0x32a5705f, v5
	v_sub_f32_e32 v22, v22, v28
	v_add_f32_e32 v22, v22, v26
	v_cvt_i32_f32_e32 v26, v28
	v_exp_f32_e32 v22, v22
	v_cmp_ngt_f32_e32 vcc, s41, v5
	v_ldexp_f32 v22, v22, v26
	s_nop 0
	v_cndmask_b32_e32 v22, 0, v22, vcc
	v_cmp_nlt_f32_e32 vcc, s42, v5
	s_nop 1
	v_cndmask_b32_e32 v5, v76, v22, vcc
	v_mul_f32_e32 v22, v5, v27
	ds_write_b32 v78, v22 offset:60
	s_and_b64 vcc, exec, s[6:7]
	v_add_f32_e64 v22, |v22|, v4
	s_cbranch_vccnz .Lhy_wout
	s_lshl_b64 s[2:3], s[2:3], 2
	v_mul_f32_e32 v4, v5, v29
	v_mov_b32_e32 v3, s3
	v_subrev_co_u32_e32 v2, vcc, s2, v24
	v_add_f32_e64 v22, |v4|, v22
	s_nop 0
	v_subb_co_u32_e32 v3, vcc, v25, v3, vcc
	ds_write_b32 v78, v4 offset:64
.Lhy_wout:
	s_and_b32 s4, s8, 16
	s_or_b32 s4, s4, s15
	s_cmpk_gt_i32 s14, 0x1ff
	s_mov_b32 s98, 0xe38000
	s_cselect_b32 s98, 0x4e28400, s98
	s_cselect_b32 s99, 11, 17
	v_readlane_b32 s100, v252, 21
	v_readlane_b32 s101, v252, 22
	v_and_b32_e32 v79, 63, v0
	v_lshrrev_b32_e32 v80, 4, v79
	v_and_b32_e32 v81, 15, v79
	v_and_b32_e32 v82, 0x1c0, v0
	v_add_u32_e32 v82, v82, v80
	v_lshlrev_b32_e32 v82, s99, v82
	v_add_u32_e32 v82, s98, v82
	v_add_u32_e32 v83, s4, v81
	v_lshl_add_u32 v84, v83, 2, v82
	v_sub_u32_e32 v85, 15, v81
	v_add_u32_e32 v85, s4, v85
	v_lshlrev_b32_e32 v86, 2, v85
	v_sub_u32_e32 v86, v82, v86
	v_cmp_ne_u32_e32 vcc, 0, v85
	s_lshl_b32 s5, 4, s99
	v_lshrrev_b32_e32 v87, 6, v0
	v_mul_u32_u24_e32 v87, 0x2100, v87
	v_mul_u32_u24_e32 v80, 0x84, v80
	v_add_u32_e32 v87, v87, v80
	v_lshl_add_u32 v87, v81, 2, v87
	v_add_u32_e32 v87, 0xa000, v87
	ds_read_b32 v26, v87 offset:0
	ds_read_b32 v27, v87 offset:528
	ds_read_b32 v28, v87 offset:1056
	ds_read_b32 v29, v87 offset:1584
	ds_read_b32 v30, v87 offset:2112
	ds_read_b32 v31, v87 offset:2640
	ds_read_b32 v32, v87 offset:3168
	ds_read_b32 v33, v87 offset:3696
	ds_read_b32 v34, v87 offset:4224
	ds_read_b32 v35, v87 offset:4752
	ds_read_b32 v36, v87 offset:5280
	ds_read_b32 v37, v87 offset:5808
	ds_read_b32 v38, v87 offset:6336
	ds_read_b32 v39, v87 offset:6864
	ds_read_b32 v40, v87 offset:7392
	ds_read_b32 v41, v87 offset:7920
	ds_read_b32 v42, v87 offset:64
	ds_read_b32 v43, v87 offset:592
	ds_read_b32 v44, v87 offset:1120
	ds_read_b32 v45, v87 offset:1648
	ds_read_b32 v46, v87 offset:2176
	ds_read_b32 v47, v87 offset:2704
	ds_read_b32 v48, v87 offset:3232
	ds_read_b32 v49, v87 offset:3760
	ds_read_b32 v50, v87 offset:4288
	ds_read_b32 v51, v87 offset:4816
	ds_read_b32 v52, v87 offset:5344
	ds_read_b32 v53, v87 offset:5872
	ds_read_b32 v54, v87 offset:6400
	ds_read_b32 v55, v87 offset:6928
	ds_read_b32 v56, v87 offset:7456
	ds_read_b32 v57, v87 offset:7984
	s_waitcnt lgkmcnt(15)
	global_store_dword v84, v26, s[100:101]
	v_add_u32_e32 v84, s5, v84
	global_store_dword v84, v27, s[100:101]
	v_add_u32_e32 v84, s5, v84
	global_store_dword v84, v28, s[100:101]
	v_add_u32_e32 v84, s5, v84
	global_store_dword v84, v29, s[100:101]
	v_add_u32_e32 v84, s5, v84
	global_store_dword v84, v30, s[100:101]
	v_add_u32_e32 v84, s5, v84
	global_store_dword v84, v31, s[100:101]
	v_add_u32_e32 v84, s5, v84
	global_store_dword v84, v32, s[100:101]
	v_add_u32_e32 v84, s5, v84
	global_store_dword v84, v33, s[100:101]
	v_add_u32_e32 v84, s5, v84
	global_store_dword v84, v34, s[100:101]
	v_add_u32_e32 v84, s5, v84
	global_store_dword v84, v35, s[100:101]
	v_add_u32_e32 v84, s5, v84
	global_store_dword v84, v36, s[100:101]
	v_add_u32_e32 v84, s5, v84
	global_store_dword v84, v37, s[100:101]
	v_add_u32_e32 v84, s5, v84
	global_store_dword v84, v38, s[100:101]
	v_add_u32_e32 v84, s5, v84
	global_store_dword v84, v39, s[100:101]
	v_add_u32_e32 v84, s5, v84
	global_store_dword v84, v40, s[100:101]
	v_add_u32_e32 v84, s5, v84
	global_store_dword v84, v41, s[100:101]
	s_waitcnt lgkmcnt(0)
	s_mov_b64 s[2:3], exec
	s_and_b64 exec, exec, vcc
	global_store_dword v86, v42, s[100:101]
	v_add_u32_e32 v86, s5, v86
	global_store_dword v86, v43, s[100:101]
	v_add_u32_e32 v86, s5, v86
	global_store_dword v86, v44, s[100:101]
	v_add_u32_e32 v86, s5, v86
	global_store_dword v86, v45, s[100:101]
	v_add_u32_e32 v86, s5, v86
	global_store_dword v86, v46, s[100:101]
	v_add_u32_e32 v86, s5, v86
	global_store_dword v86, v47, s[100:101]
	v_add_u32_e32 v86, s5, v86
	global_store_dword v86, v48, s[100:101]
	v_add_u32_e32 v86, s5, v86
	global_store_dword v86, v49, s[100:101]
	v_add_u32_e32 v86, s5, v86
	global_store_dword v86, v50, s[100:101]
	v_add_u32_e32 v86, s5, v86
	global_store_dword v86, v51, s[100:101]
	v_add_u32_e32 v86, s5, v86
	global_store_dword v86, v52, s[100:101]
	v_add_u32_e32 v86, s5, v86
	global_store_dword v86, v53, s[100:101]
	v_add_u32_e32 v86, s5, v86
	global_store_dword v86, v54, s[100:101]
	v_add_u32_e32 v86, s5, v86
	global_store_dword v86, v55, s[100:101]
	v_add_u32_e32 v86, s5, v86
	global_store_dword v86, v56, s[100:101]
	v_add_u32_e32 v86, s5, v86
	global_store_dword v86, v57, s[100:101]
	s_mov_b64 exec, s[2:3]
	s_branch .LBB0_74
